# epilogue loss reduction: low butterfly steps via DPP row rotations
# baseline (speedup 1.0000x reference)
.LBB0_455:
	v_mbcnt_hi_u32_b32 v8, -1, v176
	v_and_b32_e32 v4, 64, v8
	v_add_u32_e32 v9, 64, v4
	v_xor_b32_e32 v4, 32, v8
	v_cmp_lt_i32_e32 vcc, v4, v9
	v_cvt_f64_f32_e32 v[2:3], v167
	v_lshlrev_b32_e32 v0, 2, v0
	v_cndmask_b32_e32 v4, v8, v4, vcc
	v_lshlrev_b32_e32 v5, 2, v4
	ds_bpermute_b32 v4, v5, v2
	ds_bpermute_b32 v5, v5, v3
	v_add_u32_e32 v6, 0x20c00, v0
	s_waitcnt lgkmcnt(0)
	s_barrier
	v_add_f64 v[2:3], v[2:3], v[4:5]
	v_xor_b32_e32 v4, 16, v8
	v_cmp_lt_i32_e32 vcc, v4, v9
	ds_read_b32 v6, v6
	s_ashr_i32 s25, s24, 31
	v_cndmask_b32_e32 v4, v8, v4, vcc
	v_lshlrev_b32_e32 v5, 2, v4
	ds_bpermute_b32 v4, v5, v2
	ds_bpermute_b32 v5, v5, v3
	s_lshl_b64 s[0:1], s[24:25], 2
	s_add_u32 s0, s12, s0
	v_mov_b32_e32 v1, 0
	s_addc_u32 s1, s13, s1
	s_waitcnt lgkmcnt(0)
	v_add_f64 v[2:3], v[2:3], v[4:5]
	v_and_b32_e32 v10, 0x3ff, v6
	v_lshl_add_u64 v[6:7], s[0:1], 0, v[0:1]
	v_mov_b32_dpp v4, v2 row_ror:8 row_mask:0xf bank_mask:0xf
	v_mov_b32_dpp v5, v3 row_ror:8 row_mask:0xf bank_mask:0xf
	s_brev_b32 s0, 64
	v_cvt_f32_u32_e32 v11, v10
	v_add_f64 v[2:3], v[2:3], v[4:5]
	v_add_co_u32_e32 v6, vcc, s0, v6
	s_nop 1
	v_addc_co_u32_e32 v7, vcc, 0, v7, vcc
	v_mov_b32_dpp v4, v2 row_ror:4 row_mask:0xf bank_mask:0xf
	v_mov_b32_dpp v5, v3 row_ror:4 row_mask:0xf bank_mask:0xf
	global_store_dword v[6:7], v11, off sc0 sc1
	v_add_f64 v[2:3], v[2:3], v[4:5]
	v_mov_b32_e32 v1, 0x1f400
	v_lshl_add_u32 v1, v10, 2, v1
	v_mov_b32_dpp v4, v2 row_ror:2 row_mask:0xf bank_mask:0xf
	v_mov_b32_dpp v5, v3 row_ror:2 row_mask:0xf bank_mask:0xf
	v_mov_b32_e32 v6, 1
	ds_add_u32 v1, v6
	v_add_f64 v[2:3], v[2:3], v[4:5]
	s_mov_b32 s3, 0
	s_nop 1
	v_mov_b32_dpp v4, v2 row_ror:1 row_mask:0xf bank_mask:0xf
	v_mov_b32_dpp v5, v3 row_ror:1 row_mask:0xf bank_mask:0xf
	v_add_f64 v[2:3], v[2:3], v[4:5]
	v_cmp_eq_u32_e32 vcc, 0, v166
	s_and_saveexec_b64 s[0:1], vcc
	s_cbranch_execz .LBB0_457
	s_lshl_b32 s4, s33, 3
	s_add_i32 s4, s4, 0x21d00
	v_mov_b32_e32 v1, s4
	ds_write_b64 v1, v[2:3]
